# s9
# speedup vs baseline: 1.0648x; 1.0034x over previous
.LBB0_7:
	s_or_b64 exec, exec, s[4:5]
	s_mov_b32 s4, 0x46cc5e42
	v_mul_f64 v[4:5], v[8:9], v[8:9]
	v_mov_b32_e32 v18, 0x9037ab78
	v_mov_b32_e32 v19, 0x3e21eeb6
	s_mov_b32 s5, 0xbda907db
	v_mul_f64 v[12:13], v[4:5], 0.5
	v_fmac_f64_e32 v[18:19], s[4:5], v[4:5]
	v_mov_b32_e32 v20, 0xa17f65f6
	v_mov_b32_e32 v21, 0xbe927e4f
	v_add_f64 v[14:15], -v[12:13], 1.0
	v_fmac_f64_e32 v[20:21], v[4:5], v[18:19]
	v_mov_b32_e32 v18, 0x19f4ec90
	v_mov_b32_e32 v19, 0x3efa01a0
	v_add_f64 v[16:17], -v[14:15], 1.0
	v_fmac_f64_e32 v[18:19], v[4:5], v[20:21]
	v_mov_b32_e32 v20, 0x16c16967
	v_mov_b32_e32 v21, 0xbf56c16c
	v_add_f64 v[12:13], v[16:17], -v[12:13]
	v_fmac_f64_e32 v[20:21], v[4:5], v[18:19]
	v_mov_b32_e32 v18, 0x55555555
	v_mov_b32_e32 v19, 0x3fa55555
	v_mul_f64 v[16:17], v[4:5], v[4:5]
	v_fmac_f64_e32 v[18:19], v[4:5], v[20:21]
	v_fma_f64 v[12:13], v[8:9], -v[10:11], v[12:13]
	v_fmac_f64_e32 v[12:13], v[16:17], v[18:19]
	s_mov_b32 s6, 0xf9a43bb8
	v_add_f64 v[12:13], v[14:15], v[12:13]
	v_mov_b32_e32 v14, 0xb42fdfa7
	v_mov_b32_e32 v15, 0xbe5ae600
	s_mov_b32 s7, 0x3de5e0b2
	v_fmac_f64_e32 v[14:15], s[6:7], v[4:5]
	v_mov_b32_e32 v16, 0x796cde01
	v_mov_b32_e32 v17, 0x3ec71de3
	v_fmac_f64_e32 v[16:17], v[4:5], v[14:15]
	v_mov_b32_e32 v14, 0x19e83e5c
	v_mov_b32_e32 v15, 0xbf2a01a0
	v_fmac_f64_e32 v[14:15], v[4:5], v[16:17]
	v_mov_b32_e32 v16, 0x11110bb3
	v_mov_b32_e32 v17, 0x3f811111
	v_fmac_f64_e32 v[16:17], v[4:5], v[14:15]
	v_mul_f64 v[14:15], v[8:9], -v[4:5]
	v_mul_f64 v[18:19], v[10:11], 0.5
	s_mov_b32 s4, 0x55555555
	v_fmac_f64_e32 v[18:19], v[14:15], v[16:17]
	s_mov_b32 s5, 0xbfc55555
	v_fma_f64 v[4:5], v[4:5], v[18:19], -v[10:11]
	v_fmac_f64_e32 v[4:5], s[4:5], v[14:15]
	v_lshlrev_b32_e32 v1, 30, v3
	v_and_b32_e32 v3, 1, v3
	v_add_f64 v[4:5], v[8:9], -v[4:5]
	v_cmp_eq_u32_e32 vcc, 0, v3
	v_xor_b32_e32 v9, v1, v7
	s_brev_b32 s3, 1
	v_cndmask_b32_e32 v8, v13, v5, vcc
	v_xor_b32_e32 v5, 0x80000000, v5
	v_cndmask_b32_e32 v5, v5, v13, vcc
	v_bitop3_b32 v8, v8, v9, s3 bitop3:0x78
	v_bitop3_b32 v1, v5, v1, s3 bitop3:0x78
	s_movk_i32 s3, 0x1f8
	v_cndmask_b32_e32 v3, v12, v4, vcc
	v_cndmask_b32_e32 v4, v4, v12, vcc
	v_cmp_class_f64_e64 vcc, v[6:7], s3
	v_mov_b32_e32 v7, 0x7ff80000
	s_nop 0
	v_cndmask_b32_e32 v4, 0, v4, vcc
	v_cndmask_b32_e32 v5, v7, v1, vcc
	v_cndmask_b32_e32 v6, 0, v3, vcc
	v_cndmask_b32_e32 v7, v7, v8, vcc
	v_ashrrev_i32_e32 v3, 31, v2
	s_waitcnt lgkmcnt(0)
	v_lshl_add_u64 v[2:3], v[2:3], 3, s[8:9]
	v_cvt_f32_f64_e32 v4, v[4:5]
	v_cvt_f32_f64_e32 v5, v[6:7]
	global_store_dwordx2 v[2:3], v[4:5], off sc1
	s_branch .LBB0_2

.Lprep_go:
	s_lshl_b32 s27, s23, 12
	s_lshl_b32 s28, s22, 7
	s_add_i32 s27, s27, s28
	s_add_u32 s0, s0, s27
	s_addc_u32 s1, s1, 0
	global_load_dwordx4 v[8:11], v3, s[0:1] nt
	global_load_dwordx4 v[12:15], v3, s[0:1] offset:16 nt
	global_load_dwordx4 v[16:19], v3, s[0:1] offset:128 nt
	global_load_dwordx4 v[20:23], v3, s[0:1] offset:144 nt
	global_load_dwordx4 v[24:27], v3, s[0:1] offset:256 nt
	global_load_dwordx4 v[28:31], v3, s[0:1] offset:272 nt
	global_load_dwordx4 v[32:35], v3, s[0:1] offset:384 nt
	global_load_dwordx4 v[36:39], v3, s[0:1] offset:400 nt
	s_mul_i32 s27, s22, s25
	s_lshl_b32 s28, s24, 6
	s_add_i32 s27, s27, s28
	s_add_u32 s2, s2, s27
	s_addc_u32 s3, s3, 0
	s_add_u32 s4, s2, s25
	s_addc_u32 s5, s3, 0
	s_add_u32 s6, s4, s25
	s_addc_u32 s7, s5, 0
	s_add_u32 s8, s6, s25
	s_addc_u32 s9, s7, 0
	s_waitcnt vmcnt(6)
	v_cvt_pk_f16_f32 v8, v8, v9
	v_cvt_pk_f16_f32 v9, v10, v11
	v_cvt_pk_f16_f32 v10, v12, v13
	v_cvt_pk_f16_f32 v11, v14, v15
	global_store_dwordx4 v4, v[8:11], s[2:3] sc1
	s_waitcnt vmcnt(5)
	v_cvt_pk_f16_f32 v16, v16, v17
	v_cvt_pk_f16_f32 v17, v18, v19
	v_cvt_pk_f16_f32 v18, v20, v21
	v_cvt_pk_f16_f32 v19, v22, v23
	global_store_dwordx4 v4, v[16:19], s[4:5] sc1
	s_waitcnt vmcnt(4)
	v_cvt_pk_f16_f32 v24, v24, v25
	v_cvt_pk_f16_f32 v25, v26, v27
	v_cvt_pk_f16_f32 v26, v28, v29
	v_cvt_pk_f16_f32 v27, v30, v31
	global_store_dwordx4 v4, v[24:27], s[6:7] sc1
	s_waitcnt vmcnt(3)
	v_cvt_pk_f16_f32 v32, v32, v33
	v_cvt_pk_f16_f32 v33, v34, v35
	v_cvt_pk_f16_f32 v34, v36, v37
	v_cvt_pk_f16_f32 v35, v38, v39
	global_store_dwordx4 v4, v[32:35], s[8:9] sc1
	s_endpgm

.LBB1_34:
	v_add_u32_e32 v88, s41, v240
	ds_read_b64_tr_b16 v[80:81], v88 offset:24576
	ds_read_b64_tr_b16 v[82:83], v88 offset:25088
	v_cvt_pk_f16_f32 v64, v64, v65
	v_cvt_pk_f16_f32 v65, v66, v67
	v_cvt_pk_f16_f32 v66, v68, v69
	v_cvt_pk_f16_f32 v67, v70, v71
	ds_read_b64_tr_b16 v[68:69], v88 offset:25600
	ds_read_b64_tr_b16 v[70:71], v88 offset:26112
	s_waitcnt lgkmcnt(2)
	v_mfma_f32_32x32x16_f16 v[0:15], v[64:67], v[80:83], v[0:15]
	ds_read_b64_tr_b16 v[80:81], v88 offset:28672
	ds_read_b64_tr_b16 v[82:83], v88 offset:29184
	ds_read_b64_tr_b16 v[84:85], v88 offset:29696
	ds_read_b64_tr_b16 v[86:87], v88 offset:30208
	v_cvt_pk_f16_f32 v72, v72, v73
	v_cvt_pk_f16_f32 v73, v74, v75
	v_cvt_pk_f16_f32 v74, v76, v77
	v_cvt_pk_f16_f32 v75, v78, v79
	v_cvt_pk_f16_f32 v48, v48, v49
	v_cvt_pk_f16_f32 v49, v50, v51
	s_waitcnt lgkmcnt(2)
	v_mfma_f32_32x32x16_f16 v[16:31], v[64:67], v[80:83], v[16:31]
	v_cvt_pk_f16_f32 v50, v52, v53
	v_cvt_pk_f16_f32 v51, v54, v55
	v_cvt_pk_f16_f32 v52, v56, v57
	v_cvt_pk_f16_f32 v53, v58, v59
	v_cvt_pk_f16_f32 v54, v60, v61
	v_cvt_pk_f16_f32 v55, v62, v63
	ds_read_b64_tr_b16 v[56:57], v88 offset:26624
	ds_read_b64_tr_b16 v[58:59], v88 offset:27136
	ds_read_b64_tr_b16 v[60:61], v88 offset:27648
	ds_read_b64_tr_b16 v[62:63], v88 offset:28160
	v_mfma_f32_32x32x16_f16 v[0:15], v[72:75], v[68:71], v[0:15]
	v_pk_add_f16 v64, v64, v72
	v_pk_add_f16 v65, v65, v73
	v_pk_add_f16 v66, v66, v74
	v_pk_add_f16 v67, v67, v75
	v_pk_add_f16 v68, v48, v52
	s_lshl_b64 s[0:1], s[4:5], 1
	s_add_u32 s0, s10, s0
	s_waitcnt lgkmcnt(2)
	v_mfma_f32_32x32x16_f16 v[0:15], v[48:51], v[56:59], v[0:15]
	v_pk_add_f16 v56, v49, v53
	v_pk_add_f16 v57, v50, v54
	v_pk_add_f16 v58, v51, v55
	s_addc_u32 s1, s11, s1
	v_pk_add_f16 v59, v67, v58
	v_pk_add_f16 v58, v66, v57
	v_pk_add_f16 v57, v65, v56
	v_mfma_f32_32x32x16_f16 v[16:31], v[72:75], v[84:87], v[16:31]
	v_pk_add_f16 v56, v64, v68
	s_lshl_b32 s2, s33, 12
	s_add_i32 s2, s2, 0
	s_lshl_b32 s3, s36, 1
	s_add_u32 s0, s0, s3
	s_addc_u32 s1, s1, 0
	v_mfma_f32_32x32x16_f16 v[32:47], v[56:59], v[128:131], v[32:47]
	ds_read_b64_tr_b16 v[56:57], v88 offset:30720
	ds_read_b64_tr_b16 v[58:59], v88 offset:31232
	ds_read_b64_tr_b16 v[64:65], v88 offset:31744
	ds_read_b64_tr_b16 v[66:67], v88 offset:32256
	s_waitcnt lgkmcnt(2)
	v_mfma_f32_32x32x16_f16 v[16:31], v[48:51], v[56:59], v[16:31]
	s_nop 5
	v_rcp_f32_e32 v32, v32
	v_rcp_f32_e32 v33, v33
	v_lshl_add_u32 v48, v238, 1, s2
	v_lshlrev_b32_e32 v49, 7, v239
	v_rcp_f32_e32 v34, v34
	v_add_u32_e32 v50, v48, v49
	v_rcp_f32_e32 v35, v35
	v_mfma_f32_32x32x16_f16 v[0:15], v[52:55], v[60:63], v[0:15]
	v_rcp_f32_e32 v36, v36
	v_rcp_f32_e32 v37, v37
	v_rcp_f32_e32 v38, v38
	v_rcp_f32_e32 v39, v39
	v_rcp_f32_e32 v40, v40
	v_rcp_f32_e32 v41, v41
	v_rcp_f32_e32 v42, v42
	s_waitcnt lgkmcnt(0)
	v_mfma_f32_32x32x16_f16 v[16:31], v[52:55], v[64:67], v[16:31]
	s_nop 2
	v_fma_mixlo_f16 v0, v0, v32, 0
	ds_write_b16 v50, v0 offset:50176
	v_rcp_f32_e32 v43, v43
	v_rcp_f32_e32 v44, v44
	v_rcp_f32_e32 v45, v45
	v_rcp_f32_e32 v46, v46
	v_rcp_f32_e32 v47, v47
	s_nop 1
	v_fma_mixlo_f16 v0, v16, v32, 0
	ds_write_b16 v50, v0 offset:50240
	v_fma_mixlo_f16 v0, v1, v33, 0
	ds_write_b16 v50, v0 offset:50304
	v_fma_mixlo_f16 v0, v17, v33, 0
	ds_write_b16 v50, v0 offset:50368
	v_fma_mixlo_f16 v0, v2, v34, 0
	ds_write_b16 v50, v0 offset:50432
	v_fma_mixlo_f16 v0, v18, v34, 0
	ds_write_b16 v50, v0 offset:50496
	v_fma_mixlo_f16 v0, v3, v35, 0
	ds_write_b16 v50, v0 offset:50560
	v_fma_mixlo_f16 v0, v19, v35, 0
	ds_write_b16 v50, v0 offset:50624
	v_or_b32_e32 v0, 0x400, v49
	v_add_u32_e32 v0, v48, v0
	v_fma_mixlo_f16 v1, v4, v36, 0
	ds_write_b16 v0, v1 offset:50176
	v_fma_mixlo_f16 v1, v20, v36, 0
	ds_write_b16 v0, v1 offset:50240
	v_or_b32_e32 v0, 0x480, v49
	v_add_u32_e32 v0, v48, v0
	v_fma_mixlo_f16 v1, v5, v37, 0
	ds_write_b16 v0, v1 offset:50176
	v_fma_mixlo_f16 v1, v21, v37, 0
	ds_write_b16 v0, v1 offset:50240
	v_or_b32_e32 v0, 0x500, v49
	v_add_u32_e32 v0, v48, v0
	v_fma_mixlo_f16 v1, v6, v38, 0
	ds_write_b16 v0, v1 offset:50176
	v_fma_mixlo_f16 v1, v22, v38, 0
	ds_write_b16 v0, v1 offset:50240
	v_or_b32_e32 v0, 0x580, v49
	v_add_u32_e32 v0, v48, v0
	v_fma_mixlo_f16 v1, v7, v39, 0
	ds_write_b16 v0, v1 offset:50176
	v_fma_mixlo_f16 v1, v23, v39, 0
	ds_write_b16 v0, v1 offset:50240
	v_or_b32_e32 v0, 0x800, v49
	v_add_u32_e32 v0, v48, v0
	v_fma_mixlo_f16 v1, v8, v40, 0
	ds_write_b16 v0, v1 offset:50176
	v_fma_mixlo_f16 v1, v24, v40, 0
	ds_write_b16 v0, v1 offset:50240
	v_or_b32_e32 v0, 0x880, v49
	v_add_u32_e32 v0, v48, v0
	v_fma_mixlo_f16 v1, v9, v41, 0
	ds_write_b16 v0, v1 offset:50176
	v_fma_mixlo_f16 v1, v25, v41, 0
	ds_write_b16 v0, v1 offset:50240
	v_or_b32_e32 v0, 0x900, v49
	v_add_u32_e32 v0, v48, v0
	v_fma_mixlo_f16 v1, v10, v42, 0
	ds_write_b16 v0, v1 offset:50176
	v_fma_mixlo_f16 v1, v26, v42, 0
	ds_write_b16 v0, v1 offset:50240
	v_or_b32_e32 v0, 0x980, v49
	v_add_u32_e32 v0, v48, v0
	v_fma_mixlo_f16 v1, v11, v43, 0
	ds_write_b16 v0, v1 offset:50176
	v_fma_mixlo_f16 v1, v27, v43, 0
	ds_write_b16 v0, v1 offset:50240
	v_or_b32_e32 v0, 0xc00, v49
	v_add_u32_e32 v0, v48, v0
	v_fma_mixlo_f16 v1, v12, v44, 0
	ds_write_b16 v0, v1 offset:50176
	v_fma_mixlo_f16 v1, v28, v44, 0
	ds_write_b16 v0, v1 offset:50240
	v_or_b32_e32 v0, 0xc80, v49
	v_add_u32_e32 v0, v48, v0
	v_fma_mixlo_f16 v1, v13, v45, 0
	ds_write_b16 v0, v1 offset:50176
	v_fma_mixlo_f16 v1, v29, v45, 0
	ds_write_b16 v0, v1 offset:50240
	v_or_b32_e32 v0, 0xd00, v49
	v_add_u32_e32 v0, v48, v0
	v_fma_mixlo_f16 v1, v14, v46, 0
	ds_write_b16 v0, v1 offset:50176
	v_fma_mixlo_f16 v1, v30, v46, 0
	ds_write_b16 v0, v1 offset:50240
	v_or_b32_e32 v0, 0xd80, v49
	v_add_u32_e32 v0, v48, v0
	v_fma_mixlo_f16 v1, v15, v47, 0
	ds_write_b16 v0, v1 offset:50176
	v_fma_mixlo_f16 v1, v31, v47, 0
	ds_write_b16 v0, v1 offset:50240
	v_and_b32_e32 v0, 56, v237
	v_lshlrev_b32_e32 v8, 1, v0
	v_lshrrev_b32_e32 v14, 3, v236
	v_add_u32_e32 v15, s2, v8
	s_waitcnt lgkmcnt(0)
	v_lshl_add_u32 v0, v14, 7, v15
	v_or_b32_e32 v16, 8, v14
	ds_read_b128 v[0:3], v0 offset:50176
	v_lshl_add_u32 v4, v16, 7, v15
	ds_read_b128 v[4:7], v4 offset:50176
	v_mov_b32_e32 v9, 0
	v_lshl_add_u64 v[10:11], s[0:1], 0, v[8:9]
	v_lshlrev_b32_e32 v8, 11, v14
	v_lshl_add_u64 v[12:13], v[10:11], 0, v[8:9]
	v_lshlrev_b32_e32 v8, 11, v16
	s_waitcnt lgkmcnt(1)
	global_store_dwordx4 v[12:13], v[0:3], off sc1
	s_nop 1
	v_lshl_add_u64 v[0:1], v[10:11], 0, v[8:9]
	s_waitcnt lgkmcnt(0)
	global_store_dwordx4 v[0:1], v[4:7], off sc1
	s_nop 1
	v_or_b32_e32 v4, 16, v14
	v_lshl_add_u32 v0, v4, 7, v15
	v_or_b32_e32 v14, 24, v14
	ds_read_b128 v[0:3], v0 offset:50176
	v_lshlrev_b32_e32 v8, 11, v4
	v_lshl_add_u32 v4, v14, 7, v15
	ds_read_b128 v[4:7], v4 offset:50176
	v_lshl_add_u64 v[12:13], v[10:11], 0, v[8:9]
	v_lshlrev_b32_e32 v8, 11, v14
	s_waitcnt lgkmcnt(1)
	global_store_dwordx4 v[12:13], v[0:3], off sc1
	s_nop 1
	v_lshl_add_u64 v[0:1], v[10:11], 0, v[8:9]
	s_waitcnt lgkmcnt(0)
	global_store_dwordx4 v[0:1], v[4:7], off sc1
	s_waitcnt lgkmcnt(0)
	s_barrier
	s_endpgm

.Lepi_d0:
	s_waitcnt vmcnt(0)
	s_lshl_b32 s35, s29, 11
	v_add_u32_e32 v104, 0x8000, v0
	v_add_u32_e32 v105, 0x10000, v0
	v_add_u32_e32 v106, 0x18000, v0
	s_add_i32 s31, s34, 0
	s_lshr_b32 s30, s31, 10
	s_and_b32 s31, s31, 0x3ff
	s_lshl_b32 s31, s31, 1
	s_cmp_eq_u32 s30, 1
	s_cselect_b64 s[44:45], s[16:17], s[14:15]
	s_cmp_eq_u32 s30, 2
	s_cselect_b64 s[44:45], s[18:19], s[44:45]
	s_add_u32 s44, s44, s31
	s_addc_u32 s45, s45, 0
	s_add_u32 s44, s44, s35
	s_addc_u32 s45, s45, 0
	s_add_i32 s31, s34, 32
	s_lshr_b32 s30, s31, 10
	s_and_b32 s31, s31, 0x3ff
	s_lshl_b32 s31, s31, 1
	s_cmp_eq_u32 s30, 1
	s_cselect_b64 s[46:47], s[16:17], s[14:15]
	s_cmp_eq_u32 s30, 2
	s_cselect_b64 s[46:47], s[18:19], s[46:47]
	s_add_u32 s46, s46, s31
	s_addc_u32 s47, s47, 0
	s_add_u32 s46, s46, s35
	s_addc_u32 s47, s47, 0
	s_add_i32 s31, s34, 64
	s_lshr_b32 s30, s31, 10
	s_and_b32 s31, s31, 0x3ff
	s_lshl_b32 s31, s31, 1
	s_cmp_eq_u32 s30, 1
	s_cselect_b64 s[48:49], s[16:17], s[14:15]
	s_cmp_eq_u32 s30, 2
	s_cselect_b64 s[48:49], s[18:19], s[48:49]
	s_add_u32 s48, s48, s31
	s_addc_u32 s49, s49, 0
	s_add_u32 s48, s48, s35
	s_addc_u32 s49, s49, 0
	s_waitcnt lgkmcnt(0)
	ds_read_b128 v[2:5], v102 offset:0
	ds_read_b128 v[6:9], v102 offset:64
	ds_read_b128 v[10:13], v102 offset:128
	ds_read_b128 v[14:17], v102 offset:3328
	ds_read_b128 v[18:21], v102 offset:3392
	ds_read_b128 v[22:25], v102 offset:3456
	ds_read_b128 v[26:29], v102 offset:6656
	ds_read_b128 v[30:33], v102 offset:6720
	ds_read_b128 v[34:37], v102 offset:6784
	ds_read_b128 v[38:41], v102 offset:9984
	ds_read_b128 v[42:45], v102 offset:10048
	ds_read_b128 v[46:49], v102 offset:10112
	s_waitcnt lgkmcnt(11)
	global_store_dwordx4 v0, v[2:5], s[44:45] sc1
	s_waitcnt lgkmcnt(10)
	global_store_dwordx4 v0, v[6:9], s[46:47] sc1
	s_waitcnt lgkmcnt(9)
	global_store_dwordx4 v0, v[10:13], s[48:49] sc1
	s_waitcnt lgkmcnt(8)
	global_store_dwordx4 v104, v[14:17], s[44:45] sc1
	s_waitcnt lgkmcnt(7)
	global_store_dwordx4 v104, v[18:21], s[46:47] sc1
	s_waitcnt lgkmcnt(6)
	global_store_dwordx4 v104, v[22:25], s[48:49] sc1
	s_waitcnt lgkmcnt(5)
	global_store_dwordx4 v105, v[26:29], s[44:45] sc1
	s_waitcnt lgkmcnt(4)
	global_store_dwordx4 v105, v[30:33], s[46:47] sc1
	s_waitcnt lgkmcnt(3)
	global_store_dwordx4 v105, v[34:37], s[48:49] sc1
	s_waitcnt lgkmcnt(2)
	global_store_dwordx4 v106, v[38:41], s[44:45] sc1
	s_waitcnt lgkmcnt(1)
	global_store_dwordx4 v106, v[42:45], s[46:47] sc1
	s_waitcnt lgkmcnt(0)
	global_store_dwordx4 v106, v[46:49], s[48:49] sc1
	s_branch .LBB2_2

.LBB3_4:
	s_lshl_b32 s12, s8, 14
	s_add_i32 s12, s12, 0
	v_add3_u32 v42, s12, v37, v35
	v_add3_u32 v58, s12, v36, v35
	s_barrier
	ds_read_b128 v[38:41], v42 offset:8192
	ds_read_b128 v[42:45], v42 offset:9216
	ds_read_b128 v[46:49], v58
	ds_read_b128 v[50:53], v58 offset:1024
	ds_read_b128 v[54:57], v58 offset:2048
	ds_read_b128 v[58:61], v58 offset:3072
	s_waitcnt lgkmcnt(0)
	v_mfma_f32_16x16x32_f16 v[30:33], v[46:49], v[38:41], v[30:33]
	s_add_i32 s12, s8, 1
	s_cmp_lg_u32 s8, 4
	s_cselect_b32 s8, s12, 0
	v_mfma_f32_16x16x32_f16 v[22:25], v[46:49], v[42:45], v[22:25]
	s_add_i32 s11, s11, -1
	s_cmp_eq_u32 s11, 0
	v_mfma_f32_16x16x32_f16 v[26:29], v[50:53], v[38:41], v[26:29]
	v_mfma_f32_16x16x32_f16 v[14:17], v[50:53], v[42:45], v[14:17]
	v_mfma_f32_16x16x32_f16 v[18:21], v[54:57], v[38:41], v[18:21]
	v_mfma_f32_16x16x32_f16 v[6:9], v[54:57], v[42:45], v[6:9]
	v_mfma_f32_16x16x32_f16 v[10:13], v[58:61], v[38:41], v[10:13]
	v_mfma_f32_16x16x32_f16 v[2:5], v[58:61], v[42:45], v[2:5]
	s_cbranch_scc0 .LBB3_4
	s_or_b32 s8, s10, s4
	v_or_b32_e32 v35, s8, v34
	v_lshl_or_b32 v34, v1, 2, s9
	v_mov_b32_e32 v37, 0
	v_or_b32_e32 v34, s7, v34
	v_lshlrev_b32_e32 v36, 12, v35
	v_mov_b32_e32 v35, v37
	v_lshl_add_u64 v[38:39], s[2:3], 0, v[36:37]
	v_lshlrev_b64 v[40:41], 2, v[34:35]
	v_lshl_add_u64 v[42:43], v[38:39], 0, v[40:41]
	s_mov_b64 s[2:3], 0x10000
	v_lshl_add_u64 v[44:45], v[42:43], 0, s[2:3]
	global_store_dwordx4 v[42:43], v[30:33], off sc1
	global_store_dwordx4 v[42:43], v[26:29], off offset:64 sc1
	global_store_dwordx4 v[42:43], v[18:21], off offset:128 sc1
	global_store_dwordx4 v[42:43], v[10:13], off offset:192 sc1
	global_store_dwordx4 v[44:45], v[22:25], off sc1
	global_store_dwordx4 v[44:45], v[14:17], off offset:64 sc1
	global_store_dwordx4 v[44:45], v[6:9], off offset:128 sc1
	global_store_dwordx4 v[44:45], v[2:5], off offset:192 sc1
	s_branch .LBB3_2
